# 2 tokens per trip in input LayerNorm (16 row loads in flight per wave) with hoisted gain/bias, on top of the one-wait-state LDS-DMA blocks
# baseline (speedup 1.0000x reference)
; DI void ln_row_store(const float (&v)[32], int lane, const float* g, const float* b, float* outf, bf16_t* outb) {
;   float s = 0.f;
; #pragma unroll
;   for (int i = 0; i < 32; ++i) s += v[i];
;   s = wave_sum(s);
; DI void phase_ln_in(const Params& p, int bid, int nb) {
;     ...
;   for (int t = bid * NWAVES + wv; t < NTOK; t += nb * NWAVES) {
;     float v[32];
;     const float* xr = p.x + (size_t)t * DM;
; #pragma unroll
;     for (int i = 0; i < 8; ++i) {
;       const float4 a = *(const float4*)(xr + (i * 64 + lane) * 4);
;       v[4 * i] = a.x; v[4 * i + 1] = a.y; v[4 * i + 2] = a.z; v[4 * i + 3] = a.w;
;     }
.Lln2_top:
	v_lshl_add_u64 v[230:231], v[20:21], 0, s[4:5]
	v_lshl_add_u64 v[232:233], v[22:23], 0, s[8:9]
	global_load_dwordx4 v[24:27], v[20:21], off offset:-4096
	global_load_dwordx4 v[28:31], v[20:21], off offset:-3072
	global_load_dwordx4 v[32:35], v[20:21], off offset:-2048
	global_load_dwordx4 v[36:39], v[20:21], off offset:-1024
	global_load_dwordx4 v[64:67], v[20:21], off
	global_load_dwordx4 v[68:71], v[20:21], off offset:1024
	global_load_dwordx4 v[72:75], v[20:21], off offset:2048
	global_load_dwordx4 v[76:79], v[20:21], off offset:3072
	global_load_dwordx4 v[160:163], v[230:231], off offset:-4096
	global_load_dwordx4 v[164:167], v[230:231], off offset:-3072
	global_load_dwordx4 v[168:171], v[230:231], off offset:-2048
	global_load_dwordx4 v[172:175], v[230:231], off offset:-1024
	global_load_dwordx4 v[200:203], v[230:231], off
	global_load_dwordx4 v[204:207], v[230:231], off offset:1024
	global_load_dwordx4 v[208:211], v[230:231], off offset:2048
	global_load_dwordx4 v[212:215], v[230:231], off offset:3072
	s_waitcnt vmcnt(15)
	v_add_f32_e32 v40, 0, v24
	v_add_f32_e32 v40, v25, v40
	v_add_f32_e32 v40, v26, v40
	v_add_f32_e32 v40, v27, v40
	s_waitcnt vmcnt(14)
	v_add_f32_e32 v40, v28, v40
	v_add_f32_e32 v40, v29, v40
	v_add_f32_e32 v40, v30, v40
	v_add_f32_e32 v40, v31, v40
	s_waitcnt vmcnt(13)
	v_add_f32_e32 v40, v32, v40
	v_add_f32_e32 v40, v33, v40
	v_add_f32_e32 v40, v34, v40
	v_add_f32_e32 v40, v35, v40
	s_waitcnt vmcnt(12)
	v_add_f32_e32 v40, v36, v40
	v_add_f32_e32 v40, v37, v40
	v_add_f32_e32 v40, v38, v40
	v_add_f32_e32 v40, v39, v40
	s_waitcnt vmcnt(11)
	v_add_f32_e32 v40, v64, v40
	v_add_f32_e32 v40, v65, v40
	v_add_f32_e32 v40, v66, v40
	v_add_f32_e32 v40, v67, v40
	s_waitcnt vmcnt(10)
	v_add_f32_e32 v40, v68, v40
	v_add_f32_e32 v40, v69, v40
	v_add_f32_e32 v40, v70, v40
	v_add_f32_e32 v40, v71, v40
	s_waitcnt vmcnt(9)
	v_add_f32_e32 v40, v72, v40
	v_add_f32_e32 v40, v73, v40
	v_add_f32_e32 v40, v74, v40
	v_add_f32_e32 v40, v75, v40
	s_waitcnt vmcnt(8)
	v_add_f32_e32 v40, v76, v40
	v_add_f32_e32 v40, v77, v40
	v_add_f32_e32 v40, v78, v40
	v_add_f32_e32 v40, v79, v40
	s_waitcnt vmcnt(7)
	v_add_f32_e32 v176, 0, v160
	v_add_f32_e32 v176, v161, v176
	v_add_f32_e32 v176, v162, v176
	v_add_f32_e32 v176, v163, v176
	s_waitcnt vmcnt(6)
	v_add_f32_e32 v176, v164, v176
	v_add_f32_e32 v176, v165, v176
	v_add_f32_e32 v176, v166, v176
	v_add_f32_e32 v176, v167, v176
	s_waitcnt vmcnt(5)
	v_add_f32_e32 v176, v168, v176
	v_add_f32_e32 v176, v169, v176
	v_add_f32_e32 v176, v170, v176
	v_add_f32_e32 v176, v171, v176
	s_waitcnt vmcnt(4)
	v_add_f32_e32 v176, v172, v176
	v_add_f32_e32 v176, v173, v176
	v_add_f32_e32 v176, v174, v176
	v_add_f32_e32 v176, v175, v176
	s_waitcnt vmcnt(3)
	v_add_f32_e32 v176, v200, v176
	v_add_f32_e32 v176, v201, v176
	v_add_f32_e32 v176, v202, v176
	v_add_f32_e32 v176, v203, v176
	s_waitcnt vmcnt(2)
	v_add_f32_e32 v176, v204, v176
	v_add_f32_e32 v176, v205, v176
	v_add_f32_e32 v176, v206, v176
	v_add_f32_e32 v176, v207, v176
	s_waitcnt vmcnt(1)
	v_add_f32_e32 v176, v208, v176
	v_add_f32_e32 v176, v209, v176
	v_add_f32_e32 v176, v210, v176
	v_add_f32_e32 v176, v211, v176
	s_waitcnt vmcnt(0)
	v_add_f32_e32 v176, v212, v176
	v_add_f32_e32 v176, v213, v176
	v_add_f32_e32 v176, v214, v176
	v_add_f32_e32 v176, v215, v176
	ds_bpermute_b32 v41, v57, v40
	ds_bpermute_b32 v177, v57, v176
	s_waitcnt lgkmcnt(0)
	s_waitcnt lgkmcnt(0)
	v_add_f32_e32 v40, v40, v41
	v_add_f32_e32 v176, v176, v177
	ds_bpermute_b32 v41, v58, v40
	ds_bpermute_b32 v177, v58, v176
	s_waitcnt lgkmcnt(0)
	s_waitcnt lgkmcnt(0)
	v_add_f32_e32 v40, v40, v41
	v_add_f32_e32 v176, v176, v177
	ds_bpermute_b32 v41, v59, v40
	ds_bpermute_b32 v177, v59, v176
	s_waitcnt lgkmcnt(0)
	s_waitcnt lgkmcnt(0)
	v_add_f32_e32 v40, v40, v41
	v_add_f32_e32 v176, v176, v177
	ds_bpermute_b32 v41, v60, v40
	ds_bpermute_b32 v177, v60, v176
	s_waitcnt lgkmcnt(0)
	s_waitcnt lgkmcnt(0)
	v_add_f32_e32 v40, v40, v41
	v_add_f32_e32 v176, v176, v177
	ds_bpermute_b32 v41, v61, v40
	ds_bpermute_b32 v177, v61, v176
	s_waitcnt lgkmcnt(0)
	s_waitcnt lgkmcnt(0)
	v_add_f32_e32 v40, v40, v41
	v_add_f32_e32 v176, v176, v177
	ds_bpermute_b32 v41, v62, v40
	ds_bpermute_b32 v177, v62, v176
	s_waitcnt lgkmcnt(0)
	s_waitcnt lgkmcnt(0)
; DI void ln_row_store(const float (&v)[32], int lane, const float* g, const float* b, float* outf, bf16_t* outb) {
;     ...
;   const float mu = s * (1.f / 2048.f);
;   float q = 0.f;
; #pragma unroll
;   for (int i = 0; i < 32; ++i) { const float d = v[i] - mu; q += d * d; }
;   q = wave_sum(q);
	v_add_f32_e32 v40, v40, v41
	v_add_f32_e32 v176, v176, v177
	v_mul_f32_e32 v80, 0x3a000000, v40
	v_mul_f32_e32 v216, 0x3a000000, v176
	v_pk_add_f32 v[52:53], v[24:25], v[80:81] op_sel_hi:[1,0] neg_lo:[0,1] neg_hi:[0,1]
	v_pk_add_f32 v[188:189], v[160:161], v[216:217] op_sel_hi:[1,0] neg_lo:[0,1] neg_hi:[0,1]
	v_pk_add_f32 v[54:55], v[26:27], v[80:81] op_sel_hi:[1,0] neg_lo:[0,1] neg_hi:[0,1]
	v_pk_add_f32 v[190:191], v[162:163], v[216:217] op_sel_hi:[1,0] neg_lo:[0,1] neg_hi:[0,1]
	v_pk_add_f32 v[40:41], v[36:37], v[80:81] op_sel_hi:[1,0] neg_lo:[0,1] neg_hi:[0,1]
	v_pk_add_f32 v[176:177], v[172:173], v[216:217] op_sel_hi:[1,0] neg_lo:[0,1] neg_hi:[0,1]
	v_pk_add_f32 v[36:37], v[64:65], v[80:81] op_sel_hi:[1,0] neg_lo:[0,1] neg_hi:[0,1]
	v_pk_add_f32 v[172:173], v[200:201], v[216:217] op_sel_hi:[1,0] neg_lo:[0,1] neg_hi:[0,1]
	v_pk_mul_f32 v[64:65], v[52:53], v[52:53]
	v_pk_mul_f32 v[200:201], v[188:189], v[188:189]
	v_pk_add_f32 v[42:43], v[38:39], v[80:81] op_sel_hi:[1,0] neg_lo:[0,1] neg_hi:[0,1]
	v_pk_add_f32 v[178:179], v[174:175], v[216:217] op_sel_hi:[1,0] neg_lo:[0,1] neg_hi:[0,1]
	v_pk_add_f32 v[38:39], v[66:67], v[80:81] op_sel_hi:[1,0] neg_lo:[0,1] neg_hi:[0,1]
	v_pk_add_f32 v[174:175], v[202:203], v[216:217] op_sel_hi:[1,0] neg_lo:[0,1] neg_hi:[0,1]
	v_pk_mul_f32 v[66:67], v[54:55], v[54:55]
	v_pk_mul_f32 v[202:203], v[190:191], v[190:191]
	v_add_f32_e32 v64, v64, v65
	v_add_f32_e32 v200, v200, v201
	v_pk_add_f32 v[48:49], v[28:29], v[80:81] op_sel_hi:[1,0] neg_lo:[0,1] neg_hi:[0,1]
	v_pk_add_f32 v[184:185], v[164:165], v[216:217] op_sel_hi:[1,0] neg_lo:[0,1] neg_hi:[0,1]
	v_add_f32_e32 v64, v66, v64
	v_add_f32_e32 v200, v202, v200
	v_pk_add_f32 v[44:45], v[32:33], v[80:81] op_sel_hi:[1,0] neg_lo:[0,1] neg_hi:[0,1]
	v_pk_add_f32 v[180:181], v[168:169], v[216:217] op_sel_hi:[1,0] neg_lo:[0,1] neg_hi:[0,1]
	v_pk_add_f32 v[32:33], v[68:69], v[80:81] op_sel_hi:[1,0] neg_lo:[0,1] neg_hi:[0,1]
	v_pk_add_f32 v[168:169], v[204:205], v[216:217] op_sel_hi:[1,0] neg_lo:[0,1] neg_hi:[0,1]
	v_pk_mul_f32 v[68:69], v[48:49], v[48:49]
	v_pk_mul_f32 v[204:205], v[184:185], v[184:185]
	v_add_f32_e32 v64, v67, v64
	v_add_f32_e32 v200, v203, v200
	v_pk_add_f32 v[50:51], v[30:31], v[80:81] op_sel_hi:[1,0] neg_lo:[0,1] neg_hi:[0,1]
	v_pk_add_f32 v[186:187], v[166:167], v[216:217] op_sel_hi:[1,0] neg_lo:[0,1] neg_hi:[0,1]
	v_add_f32_e32 v64, v68, v64
	v_add_f32_e32 v200, v204, v200
	v_pk_add_f32 v[46:47], v[34:35], v[80:81] op_sel_hi:[1,0] neg_lo:[0,1] neg_hi:[0,1]
	v_pk_add_f32 v[182:183], v[170:171], v[216:217] op_sel_hi:[1,0] neg_lo:[0,1] neg_hi:[0,1]
	v_pk_add_f32 v[34:35], v[70:71], v[80:81] op_sel_hi:[1,0] neg_lo:[0,1] neg_hi:[0,1]
	v_pk_add_f32 v[170:171], v[206:207], v[216:217] op_sel_hi:[1,0] neg_lo:[0,1] neg_hi:[0,1]
	v_pk_mul_f32 v[70:71], v[50:51], v[50:51]
	v_pk_mul_f32 v[206:207], v[186:187], v[186:187]
	v_add_f32_e32 v66, v69, v64
	v_add_f32_e32 v202, v205, v200
	v_add_f32_e32 v66, v70, v66
	v_add_f32_e32 v202, v206, v202
	v_pk_add_f32 v[28:29], v[72:73], v[80:81] op_sel_hi:[1,0] neg_lo:[0,1] neg_hi:[0,1]
	v_pk_add_f32 v[164:165], v[208:209], v[216:217] op_sel_hi:[1,0] neg_lo:[0,1] neg_hi:[0,1]
	v_pk_mul_f32 v[72:73], v[44:45], v[44:45]
	v_pk_mul_f32 v[208:209], v[180:181], v[180:181]
	v_add_f32_e32 v66, v71, v66
	v_add_f32_e32 v202, v207, v202
	v_add_f32_e32 v66, v72, v66
	v_add_f32_e32 v202, v208, v202
	v_pk_add_f32 v[30:31], v[74:75], v[80:81] op_sel_hi:[1,0] neg_lo:[0,1] neg_hi:[0,1]
	v_pk_add_f32 v[166:167], v[210:211], v[216:217] op_sel_hi:[1,0] neg_lo:[0,1] neg_hi:[0,1]
	v_pk_mul_f32 v[74:75], v[46:47], v[46:47]
	v_pk_mul_f32 v[210:211], v[182:183], v[182:183]
	v_add_f32_e32 v66, v73, v66
	v_add_f32_e32 v202, v209, v202
	v_add_f32_e32 v66, v74, v66
	v_add_f32_e32 v202, v210, v202
	v_pk_add_f32 v[24:25], v[76:77], v[80:81] op_sel_hi:[1,0] neg_lo:[0,1] neg_hi:[0,1]
	v_pk_add_f32 v[160:161], v[212:213], v[216:217] op_sel_hi:[1,0] neg_lo:[0,1] neg_hi:[0,1]
	v_pk_mul_f32 v[76:77], v[40:41], v[40:41]
	v_pk_mul_f32 v[212:213], v[176:177], v[176:177]
	v_add_f32_e32 v66, v75, v66
	v_add_f32_e32 v202, v211, v202
	v_add_f32_e32 v66, v76, v66
	v_add_f32_e32 v202, v212, v202
	v_pk_add_f32 v[26:27], v[78:79], v[80:81] op_sel_hi:[1,0] neg_lo:[0,1] neg_hi:[0,1]
	v_pk_add_f32 v[162:163], v[214:215], v[216:217] op_sel_hi:[1,0] neg_lo:[0,1] neg_hi:[0,1]
	v_pk_mul_f32 v[78:79], v[42:43], v[42:43]
	v_pk_mul_f32 v[214:215], v[178:179], v[178:179]
	v_add_f32_e32 v66, v77, v66
	v_add_f32_e32 v202, v213, v202
	v_add_f32_e32 v66, v78, v66
	v_add_f32_e32 v202, v214, v202
	v_pk_mul_f32 v[80:81], v[36:37], v[36:37]
	v_pk_mul_f32 v[216:217], v[172:173], v[172:173]
	v_add_f32_e32 v66, v79, v66
	v_add_f32_e32 v202, v215, v202
	v_add_f32_e32 v66, v80, v66
	v_add_f32_e32 v202, v216, v202
	v_pk_mul_f32 v[82:83], v[38:39], v[38:39]
	v_pk_mul_f32 v[218:219], v[174:175], v[174:175]
	v_add_f32_e32 v66, v81, v66
	v_add_f32_e32 v202, v217, v202
	v_add_f32_e32 v66, v82, v66
	v_add_f32_e32 v202, v218, v202
	v_pk_mul_f32 v[84:85], v[32:33], v[32:33]
	v_pk_mul_f32 v[220:221], v[168:169], v[168:169]
	v_add_f32_e32 v66, v83, v66
	v_add_f32_e32 v202, v219, v202
	v_add_f32_e32 v66, v84, v66
	v_add_f32_e32 v202, v220, v202
	v_pk_mul_f32 v[86:87], v[34:35], v[34:35]
	v_pk_mul_f32 v[222:223], v[170:171], v[170:171]
	v_add_f32_e32 v66, v85, v66
	v_add_f32_e32 v202, v221, v202
	v_add_f32_e32 v66, v86, v66
	v_add_f32_e32 v202, v222, v202
	v_pk_mul_f32 v[88:89], v[28:29], v[28:29]
	v_pk_mul_f32 v[224:225], v[164:165], v[164:165]
	v_add_f32_e32 v66, v87, v66
	v_add_f32_e32 v202, v223, v202
	v_add_f32_e32 v66, v88, v66
	v_add_f32_e32 v202, v224, v202
	v_pk_mul_f32 v[90:91], v[30:31], v[30:31]
	v_pk_mul_f32 v[226:227], v[166:167], v[166:167]
	v_add_f32_e32 v66, v89, v66
	v_add_f32_e32 v202, v225, v202
	v_add_f32_e32 v66, v90, v66
	v_add_f32_e32 v202, v226, v202
	v_pk_mul_f32 v[92:93], v[24:25], v[24:25]
	v_pk_mul_f32 v[228:229], v[160:161], v[160:161]
	v_add_f32_e32 v66, v91, v66
	v_add_f32_e32 v202, v227, v202
	v_add_f32_e32 v66, v92, v66
	v_add_f32_e32 v202, v228, v202
	v_pk_mul_f32 v[64:65], v[26:27], v[26:27]
	v_pk_mul_f32 v[200:201], v[162:163], v[162:163]
	v_add_f32_e32 v66, v93, v66
	v_add_f32_e32 v202, v229, v202
	v_add_f32_e32 v64, v64, v66
	v_add_f32_e32 v200, v200, v202
	v_add_f32_e32 v64, v65, v64
	v_add_f32_e32 v200, v201, v200
	ds_bpermute_b32 v65, v57, v64
	ds_bpermute_b32 v201, v57, v200
	s_waitcnt lgkmcnt(0)
; DI void ln_row_store(const float (&v)[32], int lane, const float* g, const float* b, float* outf, bf16_t* outb) {
;     ...
;   q = wave_sum(q);
;   const float rs = rsqrtf(q * (1.f / 2048.f) + LN_EPS);
; #pragma unroll
;   for (int i = 0; i < 8; ++i) {
;     const int c = (i * 64 + lane) * 4;
;     const float4 gg = *(const float4*)(g + c);
;     const float4 bb = *(const float4*)(b + c);
;     float4 o;
;     o.x = (v[4 * i + 0] - mu) * rs * gg.x + bb.x;
;     o.y = (v[4 * i + 1] - mu) * rs * gg.y + bb.y;
;     o.z = (v[4 * i + 2] - mu) * rs * gg.z + bb.z;
;     o.w = (v[4 * i + 3] - mu) * rs * gg.w + bb.w;
;     if (outf) *(float4*)(outf + c) = o;
;     if (outb) { uint2 pk; pk.x = pack2(o.x, o.y); pk.y = pack2(o.z, o.w); *(uint2*)(outb + c) = pk; }
	s_waitcnt lgkmcnt(0)
	v_add_f32_e32 v64, v64, v65
	v_add_f32_e32 v200, v200, v201
	ds_bpermute_b32 v65, v58, v64
	ds_bpermute_b32 v201, v58, v200
	s_waitcnt lgkmcnt(0)
	s_waitcnt lgkmcnt(0)
	v_add_f32_e32 v64, v64, v65
	v_add_f32_e32 v200, v200, v201
	ds_bpermute_b32 v65, v59, v64
	ds_bpermute_b32 v201, v59, v200
	s_waitcnt lgkmcnt(0)
	s_waitcnt lgkmcnt(0)
	v_add_f32_e32 v64, v64, v65
	v_add_f32_e32 v200, v200, v201
	ds_bpermute_b32 v65, v60, v64
	ds_bpermute_b32 v201, v60, v200
	s_waitcnt lgkmcnt(0)
	s_waitcnt lgkmcnt(0)
	v_add_f32_e32 v64, v64, v65
	v_add_f32_e32 v200, v200, v201
	ds_bpermute_b32 v65, v61, v64
	ds_bpermute_b32 v201, v61, v200
	s_waitcnt lgkmcnt(0)
	s_waitcnt lgkmcnt(0)
	v_add_f32_e32 v64, v64, v65
	v_add_f32_e32 v200, v200, v201
	ds_bpermute_b32 v65, v62, v64
	ds_bpermute_b32 v201, v62, v200
	s_waitcnt lgkmcnt(0)
	s_waitcnt lgkmcnt(0)
	v_add_f32_e32 v64, v64, v65
	v_add_f32_e32 v200, v200, v201
	v_fmamk_f32 v64, v64, 0x3a000000, v63
	s_mov_b32 s0, 0x800000
	v_mul_f32_e32 v65, 0x4b800000, v64
	v_cmp_gt_f32_e32 vcc, s0, v64
	s_nop 1
	v_cndmask_b32_e32 v64, v64, v65, vcc
	v_rsq_f32_e32 v64, v64
	s_nop 0
	v_mul_f32_e32 v65, 0x45800000, v64
	v_cndmask_b32_e32 v74, v64, v65, vcc
	v_fmamk_f32 v200, v200, 0x3a000000, v63
	s_mov_b32 s0, 0x800000
	v_mul_f32_e32 v201, 0x4b800000, v200
	v_cmp_gt_f32_e32 vcc, s0, v200
	s_nop 1
	v_cndmask_b32_e32 v200, v200, v201, vcc
	v_rsq_f32_e32 v200, v200
	s_nop 0
	v_mul_f32_e32 v201, 0x45800000, v200
	v_cndmask_b32_e32 v210, v200, v201, vcc
	v_pk_mul_f32 v[54:55], v[54:55], v[74:75] op_sel_hi:[1,0]
	v_pk_mul_f32 v[190:191], v[190:191], v[210:211] op_sel_hi:[1,0]
	v_pk_mul_f32 v[52:53], v[52:53], v[74:75] op_sel_hi:[1,0]
	v_pk_mul_f32 v[188:189], v[188:189], v[210:211] op_sel_hi:[1,0]
	v_pk_mul_f32 v[50:51], v[50:51], v[74:75] op_sel_hi:[1,0]
	v_pk_mul_f32 v[186:187], v[186:187], v[210:211] op_sel_hi:[1,0]
	v_pk_mul_f32 v[48:49], v[48:49], v[74:75] op_sel_hi:[1,0]
	v_pk_mul_f32 v[184:185], v[184:185], v[210:211] op_sel_hi:[1,0]
	v_pk_mul_f32 v[46:47], v[46:47], v[74:75] op_sel_hi:[1,0]
	v_pk_mul_f32 v[182:183], v[182:183], v[210:211] op_sel_hi:[1,0]
	v_pk_mul_f32 v[44:45], v[44:45], v[74:75] op_sel_hi:[1,0]
	v_pk_mul_f32 v[180:181], v[180:181], v[210:211] op_sel_hi:[1,0]
	v_pk_mul_f32 v[42:43], v[42:43], v[74:75] op_sel_hi:[1,0]
	v_pk_mul_f32 v[178:179], v[178:179], v[210:211] op_sel_hi:[1,0]
	v_pk_mul_f32 v[40:41], v[40:41], v[74:75] op_sel_hi:[1,0]
	v_pk_mul_f32 v[176:177], v[176:177], v[210:211] op_sel_hi:[1,0]
	v_pk_mul_f32 v[38:39], v[38:39], v[74:75] op_sel_hi:[1,0]
	v_pk_mul_f32 v[174:175], v[174:175], v[210:211] op_sel_hi:[1,0]
	v_pk_mul_f32 v[36:37], v[36:37], v[74:75] op_sel_hi:[1,0]
	v_pk_mul_f32 v[172:173], v[172:173], v[210:211] op_sel_hi:[1,0]
	v_pk_mul_f32 v[34:35], v[34:35], v[74:75] op_sel_hi:[1,0]
	v_pk_mul_f32 v[170:171], v[170:171], v[210:211] op_sel_hi:[1,0]
	v_pk_mul_f32 v[32:33], v[32:33], v[74:75] op_sel_hi:[1,0]
	v_pk_mul_f32 v[168:169], v[168:169], v[210:211] op_sel_hi:[1,0]
	v_pk_mul_f32 v[30:31], v[30:31], v[74:75] op_sel_hi:[1,0]
	v_pk_mul_f32 v[166:167], v[166:167], v[210:211] op_sel_hi:[1,0]
	v_pk_mul_f32 v[28:29], v[28:29], v[74:75] op_sel_hi:[1,0]
	v_pk_mul_f32 v[164:165], v[164:165], v[210:211] op_sel_hi:[1,0]
	v_pk_mul_f32 v[26:27], v[26:27], v[74:75] op_sel_hi:[1,0]
	v_pk_mul_f32 v[162:163], v[162:163], v[210:211] op_sel_hi:[1,0]
	v_pk_mul_f32 v[24:25], v[24:25], v[74:75] op_sel_hi:[1,0]
	v_pk_mul_f32 v[160:161], v[160:161], v[210:211] op_sel_hi:[1,0]
	v_pk_fma_f32 v[54:55], v[54:55], v[98:99], v[102:103]
	v_pk_fma_f32 v[190:191], v[190:191], v[98:99], v[102:103]
	v_pk_fma_f32 v[52:53], v[52:53], v[96:97], v[100:101]
	v_pk_fma_f32 v[188:189], v[188:189], v[96:97], v[100:101]
	s_nop 0
	s_nop 0
	v_cvt_pk_bf16_f32 v52, v52, v53
	v_cvt_pk_bf16_f32 v188, v188, v189
	v_cvt_pk_bf16_f32 v53, v54, v55
	v_cvt_pk_bf16_f32 v189, v190, v191
	global_store_dwordx2 v[22:23], v[52:53], off
	global_store_dwordx2 v[232:233], v[188:189], off
; #define OPAQUE_TID(P) (((P).wid0 << 6) | lane_id_now())
; DI void ln_row_store(const float (&v)[32], int lane, const float* g, const float* b, float* outf, bf16_t* outb) {
;     ...
; #pragma unroll
;   for (int i = 0; i < 8; ++i) {
;     const int c = (i * 64 + lane) * 4;
;     const float4 gg = *(const float4*)(g + c);
;     const float4 bb = *(const float4*)(b + c);
;     float4 o;
;     o.x = (v[4 * i + 0] - mu) * rs * gg.x + bb.x;
;     o.y = (v[4 * i + 1] - mu) * rs * gg.y + bb.y;
;     o.z = (v[4 * i + 2] - mu) * rs * gg.z + bb.z;
;     o.w = (v[4 * i + 3] - mu) * rs * gg.w + bb.w;
;     if (outf) *(float4*)(outf + c) = o;
;     if (outb) { uint2 pk; pk.x = pack2(o.x, o.y); pk.y = pack2(o.z, o.w); *(uint2*)(outb + c) = pk; }
;   }
; }
; DI void phase_ln_in(const Params& p, int bid, int nb) {
;   const int tid_ = OPAQUE_TID(p), lane = tid_ & 63, wv = tid_ >> 6;
;   for (int t = bid * NWAVES + wv; t < NTOK; t += nb * NWAVES) {
	v_pk_fma_f32 v[50:51], v[50:51], v[106:107], v[110:111]
	v_pk_fma_f32 v[186:187], v[186:187], v[106:107], v[110:111]
	v_pk_fma_f32 v[48:49], v[48:49], v[104:105], v[108:109]
	v_pk_fma_f32 v[184:185], v[184:185], v[104:105], v[108:109]
	s_nop 0
	s_nop 0
	v_cvt_pk_bf16_f32 v48, v48, v49
	v_cvt_pk_bf16_f32 v184, v184, v185
	v_cvt_pk_bf16_f32 v49, v50, v51
	v_cvt_pk_bf16_f32 v185, v186, v187
	global_store_dwordx2 v[22:23], v[48:49], off offset:512
	global_store_dwordx2 v[232:233], v[184:185], off offset:512
	v_pk_fma_f32 v[46:47], v[46:47], v[114:115], v[118:119]
	v_pk_fma_f32 v[182:183], v[182:183], v[114:115], v[118:119]
	v_pk_fma_f32 v[44:45], v[44:45], v[112:113], v[116:117]
	v_pk_fma_f32 v[180:181], v[180:181], v[112:113], v[116:117]
	s_nop 0
	s_nop 0
	v_cvt_pk_bf16_f32 v44, v44, v45
	v_cvt_pk_bf16_f32 v180, v180, v181
	v_cvt_pk_bf16_f32 v45, v46, v47
	v_cvt_pk_bf16_f32 v181, v182, v183
	global_store_dwordx2 v[22:23], v[44:45], off offset:1024
	global_store_dwordx2 v[232:233], v[180:181], off offset:1024
	v_pk_fma_f32 v[42:43], v[42:43], v[122:123], v[126:127]
	v_pk_fma_f32 v[178:179], v[178:179], v[122:123], v[126:127]
	v_pk_fma_f32 v[40:41], v[40:41], v[120:121], v[124:125]
	v_pk_fma_f32 v[176:177], v[176:177], v[120:121], v[124:125]
	s_nop 0
	s_nop 0
	v_cvt_pk_bf16_f32 v40, v40, v41
	v_cvt_pk_bf16_f32 v176, v176, v177
	v_cvt_pk_bf16_f32 v41, v42, v43
	v_cvt_pk_bf16_f32 v177, v178, v179
	global_store_dwordx2 v[22:23], v[40:41], off offset:1536
	global_store_dwordx2 v[232:233], v[176:177], off offset:1536
	v_pk_fma_f32 v[38:39], v[38:39], v[130:131], v[134:135]
	v_pk_fma_f32 v[174:175], v[174:175], v[130:131], v[134:135]
	v_pk_fma_f32 v[36:37], v[36:37], v[128:129], v[132:133]
	v_pk_fma_f32 v[172:173], v[172:173], v[128:129], v[132:133]
	s_nop 0
	s_nop 0
	v_cvt_pk_bf16_f32 v36, v36, v37
	v_cvt_pk_bf16_f32 v172, v172, v173
	v_cvt_pk_bf16_f32 v37, v38, v39
	v_cvt_pk_bf16_f32 v173, v174, v175
	global_store_dwordx2 v[22:23], v[36:37], off offset:2048
	global_store_dwordx2 v[232:233], v[172:173], off offset:2048
	v_pk_fma_f32 v[34:35], v[34:35], v[138:139], v[142:143]
	v_pk_fma_f32 v[170:171], v[170:171], v[138:139], v[142:143]
	v_pk_fma_f32 v[32:33], v[32:33], v[136:137], v[140:141]
	v_pk_fma_f32 v[168:169], v[168:169], v[136:137], v[140:141]
	s_nop 0
	s_nop 0
	v_cvt_pk_bf16_f32 v32, v32, v33
	v_cvt_pk_bf16_f32 v168, v168, v169
	v_cvt_pk_bf16_f32 v33, v34, v35
	v_cvt_pk_bf16_f32 v169, v170, v171
	global_store_dwordx2 v[22:23], v[32:33], off offset:2560
	global_store_dwordx2 v[232:233], v[168:169], off offset:2560
	v_pk_fma_f32 v[30:31], v[30:31], v[146:147], v[150:151]
	v_pk_fma_f32 v[166:167], v[166:167], v[146:147], v[150:151]
	v_pk_fma_f32 v[28:29], v[28:29], v[144:145], v[148:149]
	v_pk_fma_f32 v[164:165], v[164:165], v[144:145], v[148:149]
	s_nop 0
	s_nop 0
	v_cvt_pk_bf16_f32 v28, v28, v29
	v_cvt_pk_bf16_f32 v164, v164, v165
	v_cvt_pk_bf16_f32 v29, v30, v31
	v_cvt_pk_bf16_f32 v165, v166, v167
	global_store_dwordx2 v[22:23], v[28:29], off offset:3072
	global_store_dwordx2 v[232:233], v[164:165], off offset:3072
	v_pk_fma_f32 v[26:27], v[26:27], v[154:155], v[158:159]
	v_pk_fma_f32 v[162:163], v[162:163], v[154:155], v[158:159]
	v_pk_fma_f32 v[24:25], v[24:25], v[152:153], v[156:157]
	v_pk_fma_f32 v[160:161], v[160:161], v[152:153], v[156:157]
	s_nop 0
	s_nop 0
	v_cvt_pk_bf16_f32 v24, v24, v25
	v_cvt_pk_bf16_f32 v160, v160, v161
	v_cvt_pk_bf16_f32 v25, v26, v27
	v_cvt_pk_bf16_f32 v161, v162, v163
	global_store_dwordx2 v[22:23], v[24:25], off offset:3584
	global_store_dwordx2 v[232:233], v[160:161], off offset:3584
	v_lshl_add_u32 v56, s26, 1, v56
	v_lshl_add_u64 v[20:21], v[230:231], 0, s[4:5]
	v_lshl_add_u64 v[22:23], v[232:233], 0, s[8:9]
.Lln2_chk:
	v_add_u32_e32 v94, s26, v56
	s_movk_i32 s0, 0x1fff
	v_cmp_lt_i32_e32 vcc, s0, v94
	s_cbranch_vccz .Lln2_top
	v_cmp_lt_i32_e32 vcc, s0, v56
	s_or_b64 s[28:29], vcc, s[28:29]
	s_andn2_b64 exec, exec, s[28:29]
	s_cbranch_execz .LBB0_18
	s_branch .LBB0_16
